# v23 + P6 K-loop: packed-fp8 carry kept in v40-43 (8-12 v_mov per iteration removed from the load segment; copies only at loop entry/exit)
# baseline (speedup 1.0000x reference)
.LBB0_923:
	s_add_i32 s3, s94, 0x180
	s_add_i32 s4, s36, 0x180
	s_waitcnt lgkmcnt(0)
	s_barrier
	s_setprio 1
	v_mfma_scale_f32_16x16x128_f8f6f4 v[124:127], v[24:31], v[56:63], 0, v213, v213 op_sel_hi:[0,0,0]
	v_mfma_scale_f32_16x16x128_f8f6f4 v[120:123], v[16:23], v[56:63], 0, v213, v213 op_sel_hi:[0,0,0]
	v_mfma_scale_f32_16x16x128_f8f6f4 v[116:119], v[24:31], v[48:55], 0, v213, v213 op_sel_hi:[0,0,0]
	v_mfma_scale_f32_16x16x128_f8f6f4 v[112:115], v[16:23], v[48:55], 0, v213, v213 op_sel_hi:[0,0,0]
	v_mfma_scale_f32_16x16x128_f8f6f4 v[108:111], v[24:31], v[40:47], 0, v213, v213 op_sel_hi:[0,0,0]
	v_mfma_scale_f32_16x16x128_f8f6f4 v[104:107], v[16:23], v[40:47], 0, v213, v213 op_sel_hi:[0,0,0]
	v_mfma_scale_f32_16x16x128_f8f6f4 v[100:103], v[24:31], v[32:39], 0, v213, v213 op_sel_hi:[0,0,0]
	v_mfma_scale_f32_16x16x128_f8f6f4 v[96:99], v[16:23], v[32:39], 0, v213, v213 op_sel_hi:[0,0,0]
	s_setprio 0
	s_setprio 1
	v_mfma_scale_f32_16x16x128_f8f6f4 v[92:95], v[8:15], v[56:63], 0, v213, v213 op_sel_hi:[0,0,0]
	v_mfma_scale_f32_16x16x128_f8f6f4 v[88:91], v[0:7], v[56:63], 0, v213, v213 op_sel_hi:[0,0,0]
	v_mfma_scale_f32_16x16x128_f8f6f4 v[84:87], v[8:15], v[48:55], 0, v213, v213 op_sel_hi:[0,0,0]
	v_mfma_scale_f32_16x16x128_f8f6f4 v[80:83], v[0:7], v[48:55], 0, v213, v213 op_sel_hi:[0,0,0]
	v_mfma_scale_f32_16x16x128_f8f6f4 v[76:79], v[8:15], v[40:47], 0, v213, v213 op_sel_hi:[0,0,0]
	v_mfma_scale_f32_16x16x128_f8f6f4 v[72:75], v[0:7], v[40:47], 0, v213, v213 op_sel_hi:[0,0,0]
	v_mfma_scale_f32_16x16x128_f8f6f4 v[68:71], v[8:15], v[32:39], 0, v213, v213 op_sel_hi:[0,0,0]
	v_mfma_scale_f32_16x16x128_f8f6f4 v[64:67], v[0:7], v[32:39], 0, v213, v213 op_sel_hi:[0,0,0]
	s_setprio 0
	s_barrier
	ds_read_b128 v[24:27], v217 offset:0x8000
	ds_read_b128 v[28:31], v217 offset:0x8400
	ds_read_b128 v[16:19], v217 offset:0x8800
	ds_read_b128 v[20:23], v217 offset:0x8c00
	ds_read_b128 v[32:35], v216 offset:0x8000
	ds_read_b128 v[36:39], v216 offset:0x8400
	ds_read_b128 v[40:43], v216 offset:0x8800
	ds_read_b128 v[44:47], v216 offset:0x8c00
	ds_read_b128 v[48:51], v216 offset:0x9000
	ds_read_b128 v[52:55], v216 offset:0x9400
	ds_read_b128 v[56:59], v216 offset:0x9800
	ds_read_b128 v[60:63], v216 offset:0x9c00
	ds_read_b128 v[8:11], v217 offset:0xc000
	ds_read_b128 v[12:15], v217 offset:0xc400
	ds_read_b128 v[0:3], v217 offset:0xc800
	ds_read_b128 v[4:7], v217 offset:0xcc00
	s_mov_b32 m0, s76
	s_add_i32 s5, s94, 0x80100
	buffer_load_dwordx4 v214, s[12:15], s5 offen lds
	s_add_i32 s5, s94, 0xc0100
	s_mov_b32 m0, s77
	s_nop 0
	buffer_load_dwordx4 v214, s[12:15], s5 offen lds
	s_waitcnt vmcnt(10)
	s_waitcnt lgkmcnt(4)
	s_barrier
	s_setprio 1
	v_mfma_scale_f32_16x16x128_f8f6f4 v[188:191], v[24:31], v[32:39], v[188:191], v213, v213 op_sel_hi:[0,0,0]
	v_mfma_scale_f32_16x16x128_f8f6f4 v[184:187], v[16:23], v[32:39], v[184:187], v213, v213 op_sel_hi:[0,0,0]
	v_mfma_scale_f32_16x16x128_f8f6f4 v[180:183], v[24:31], v[40:47], v[180:183], v213, v213 op_sel_hi:[0,0,0]
	v_mfma_scale_f32_16x16x128_f8f6f4 v[176:179], v[16:23], v[40:47], v[176:179], v213, v213 op_sel_hi:[0,0,0]
	v_mfma_scale_f32_16x16x128_f8f6f4 v[172:175], v[24:31], v[48:55], v[172:175], v213, v213 op_sel_hi:[0,0,0]
	v_mfma_scale_f32_16x16x128_f8f6f4 v[168:171], v[16:23], v[48:55], v[168:171], v213, v213 op_sel_hi:[0,0,0]
	v_mfma_scale_f32_16x16x128_f8f6f4 v[164:167], v[24:31], v[56:63], v[164:167], v213, v213 op_sel_hi:[0,0,0]
	v_mfma_scale_f32_16x16x128_f8f6f4 v[160:163], v[16:23], v[56:63], v[160:163], v213, v213 op_sel_hi:[0,0,0]
	s_setprio 0
	s_setprio 1
	s_waitcnt lgkmcnt(2)
	v_mfma_scale_f32_16x16x128_f8f6f4 v[156:159], v[8:15], v[32:39], v[156:159], v213, v213 op_sel_hi:[0,0,0]
	s_waitcnt lgkmcnt(0)
	v_mfma_scale_f32_16x16x128_f8f6f4 v[152:155], v[0:7], v[32:39], v[152:155], v213, v213 op_sel_hi:[0,0,0]
	v_mfma_scale_f32_16x16x128_f8f6f4 v[148:151], v[8:15], v[40:47], v[148:151], v213, v213 op_sel_hi:[0,0,0]
	v_mfma_scale_f32_16x16x128_f8f6f4 v[144:147], v[0:7], v[40:47], v[144:147], v213, v213 op_sel_hi:[0,0,0]
	v_mfma_scale_f32_16x16x128_f8f6f4 v[140:143], v[8:15], v[48:55], v[140:143], v213, v213 op_sel_hi:[0,0,0]
	v_mfma_scale_f32_16x16x128_f8f6f4 v[136:139], v[0:7], v[48:55], v[136:139], v213, v213 op_sel_hi:[0,0,0]
	v_mfma_scale_f32_16x16x128_f8f6f4 v[132:135], v[8:15], v[56:63], v[132:135], v213, v213 op_sel_hi:[0,0,0]
	v_mfma_scale_f32_16x16x128_f8f6f4 v[128:131], v[0:7], v[56:63], v[128:131], v213, v213 op_sel_hi:[0,0,0]
	s_setprio 0
	s_barrier
	ds_read_b128 v[32:35], v216 offset:0xc000
	ds_read_b128 v[36:39], v216 offset:0xc400
	ds_read_b128 v[40:43], v216 offset:0xc800
	ds_read_b128 v[44:47], v216 offset:0xcc00
	ds_read_b128 v[48:51], v216 offset:0xd000
	ds_read_b128 v[52:55], v216 offset:0xd400
	ds_read_b128 v[56:59], v216 offset:0xd800
	ds_read_b128 v[60:63], v216 offset:0xdc00
	s_mov_b32 m0, s80
	s_mov_b32 s10, s14
	s_mov_b32 s11, s15
	buffer_load_dwordx4 v215, s[8:11], s4 offen lds
	s_add_i32 s4, s36, 0x80180
	s_mov_b32 m0, s81
	s_nop 0
	buffer_load_dwordx4 v215, s[8:11], s4 offen lds
	s_add_i32 s4, s36, 0x8180
	s_mov_b32 m0, s84
	s_nop 0
	buffer_load_dwordx4 v215, s[8:11], s4 offen lds
	s_add_i32 s4, s36, 0x88180
	s_mov_b32 m0, s85
	s_nop 0
	buffer_load_dwordx4 v215, s[8:11], s4 offen lds
	s_mov_b32 m0, s82
	s_nop 0
	buffer_load_dwordx4 v214, s[12:15], s3 offen lds
	s_add_i32 s3, s94, 0x40180
	s_mov_b32 m0, s83
	s_nop 0
	buffer_load_dwordx4 v214, s[12:15], s3 offen lds
	s_waitcnt vmcnt(8)
	s_waitcnt lgkmcnt(0)
	s_barrier
	s_setprio 1
	v_mfma_scale_f32_16x16x128_f8f6f4 v[124:127], v[24:31], v[32:39], v[124:127], v213, v213 op_sel_hi:[0,0,0]
	v_mfma_scale_f32_16x16x128_f8f6f4 v[120:123], v[16:23], v[32:39], v[120:123], v213, v213 op_sel_hi:[0,0,0]
	v_mfma_scale_f32_16x16x128_f8f6f4 v[116:119], v[24:31], v[40:47], v[116:119], v213, v213 op_sel_hi:[0,0,0]
	v_mfma_scale_f32_16x16x128_f8f6f4 v[112:115], v[16:23], v[40:47], v[112:115], v213, v213 op_sel_hi:[0,0,0]
	v_mfma_scale_f32_16x16x128_f8f6f4 v[108:111], v[24:31], v[48:55], v[108:111], v213, v213 op_sel_hi:[0,0,0]
	v_mfma_scale_f32_16x16x128_f8f6f4 v[104:107], v[16:23], v[48:55], v[104:107], v213, v213 op_sel_hi:[0,0,0]
	v_mfma_scale_f32_16x16x128_f8f6f4 v[100:103], v[24:31], v[56:63], v[100:103], v213, v213 op_sel_hi:[0,0,0]
	v_mfma_scale_f32_16x16x128_f8f6f4 v[96:99], v[16:23], v[56:63], v[96:99], v213, v213 op_sel_hi:[0,0,0]
	s_setprio 0
	s_setprio 1
	v_mfma_scale_f32_16x16x128_f8f6f4 v[92:95], v[8:15], v[32:39], v[92:95], v213, v213 op_sel_hi:[0,0,0]
	v_mfma_scale_f32_16x16x128_f8f6f4 v[88:91], v[0:7], v[32:39], v[88:91], v213, v213 op_sel_hi:[0,0,0]
	v_mfma_scale_f32_16x16x128_f8f6f4 v[84:87], v[8:15], v[40:47], v[84:87], v213, v213 op_sel_hi:[0,0,0]
	v_mfma_scale_f32_16x16x128_f8f6f4 v[80:83], v[0:7], v[40:47], v[80:83], v213, v213 op_sel_hi:[0,0,0]
	v_mfma_scale_f32_16x16x128_f8f6f4 v[76:79], v[8:15], v[48:55], v[76:79], v213, v213 op_sel_hi:[0,0,0]
	v_mfma_scale_f32_16x16x128_f8f6f4 v[72:75], v[0:7], v[48:55], v[72:75], v213, v213 op_sel_hi:[0,0,0]
	v_mfma_scale_f32_16x16x128_f8f6f4 v[68:71], v[8:15], v[56:63], v[68:71], v213, v213 op_sel_hi:[0,0,0]
	v_mfma_scale_f32_16x16x128_f8f6f4 v[64:67], v[0:7], v[56:63], v[64:67], v213, v213 op_sel_hi:[0,0,0]
	s_setprio 0
	s_barrier
	s_waitcnt vmcnt(14)
	v_mul_f32_e32 v0, 0x42800000, v196
	v_mul_f32_e32 v1, 0x42800000, v192
	v_mul_f32_e32 v2, 0x42800000, v197
	v_mul_f32_e32 v3, 0x42800000, v193
	v_mul_f32_e32 v4, 0x42800000, v198
	v_mul_f32_e32 v5, 0x42800000, v194
	v_mul_f32_e32 v6, 0x42800000, v199
	v_mul_f32_e32 v7, 0x42800000, v195
	v_cvt_pk_fp8_f32 v202, v1, v0
	v_cvt_pk_fp8_f32 v219, v3, v2
	v_cvt_pk_fp8_f32 v220, v5, v4
	v_cvt_pk_fp8_f32 v221, v7, v6
	s_add_i32 s61, s36, 0x200
	s_mov_b32 s33, 0
	s_mov_b32 s79, s66
	s_mov_b32 s90, s68
	s_branch .LBB0_926
.LBB0_926:
	v_mov_b32_e32 v40, v202
	v_mov_b32_e32 v41, v219
	v_mov_b32_e32 v42, v220
	v_mov_b32_e32 v43, v221
.Lp6_top:
	s_add_i32 s4, s94, s33
	s_mov_b32 s64, s90
	s_add_i32 s90, s90, 1
	s_add_i32 s3, s4, 0x200
	s_add_i32 s5, s61, s33
	ds_read_b128 v[24:27], v217 offset:0
	ds_read_b128 v[28:31], v217 offset:0x400
	ds_read_b128 v[16:19], v217 offset:0x800
	ds_read_b128 v[20:23], v217 offset:0xc00
	ds_read_b128 v[46:49], v216 offset:0
	ds_read_b128 v[50:53], v216 offset:0x400
	ds_read_b128 v[54:57], v216 offset:0x800
	ds_read_b128 v[58:61], v216 offset:0xc00
	ds_read_b128 v[192:195], v216 offset:0x1000
	ds_read_b128 v[196:199], v216 offset:0x1400
	ds_read_b128 v[220:223], v216 offset:0x1800
	ds_read_b128 v[224:227], v216 offset:0x1c00
	ds_read_b128 v[8:11], v217 offset:0x4000
	ds_read_b128 v[12:15], v217 offset:0x4400
	ds_read_b128 v[0:3], v217 offset:0x4800
	ds_read_b128 v[4:7], v217 offset:0x4c00
	s_cmpk_eq_i32 s33, 0xe00
	s_cselect_b32 s65, s60, s3
	s_cselect_b32 s16, s95, s5
	s_add_i32 s3, s65, 0x80
	s_mov_b32 m0, s86
	s_add_i32 s5, s4, 0x80180
	buffer_load_dwordx4 v214, s[12:15], s5 offen lds
	s_add_i32 s4, s4, 0xc0180
	s_mov_b32 m0, s89
	s_add_i32 s17, s16, 0x80
	buffer_load_dwordx4 v214, s[12:15], s4 offen lds
	s_lshr_b32 s4, s90, 2
	s_mul_i32 s5, s4, s34
	s_add_i32 s36, s5, s2
	s_cmp_lt_i32 s4, s47
	s_cselect_b64 s[4:5], -1, 0
	s_and_b64 s[62:63], s[4:5], exec
	s_cselect_b32 s67, s36, 0
	s_ashr_i32 s62, s67, 7
	s_bfe_u32 s36, s90, 0x10001
	s_ashr_i32 s63, s62, 31
	s_or_b32 s78, s36, s87
	s_bfe_u32 s36, s67, 0x20005
	s_lshl_b64 vcc, s[62:63], 23
	s_add_u32 vcc_lo, s28, vcc_lo
	s_addc_u32 vcc_hi, s29, vcc_hi
	s_lshl_b32 s38, s36, 21
	s_add_u32 s38, vcc_lo, s38
	s_addc_u32 s39, vcc_hi, 0
	s_lshl_b32 s67, s67, 7
	s_and_b32 s67, s67, 0xf80
	s_lshl_b32 vcc_lo, s67, 2
	s_add_u32 vcc_lo, s38, vcc_lo
	v_and_or_b32 v202, s79, 2, v200
	s_addc_u32 vcc_hi, s39, 0
	v_lshl_or_b32 v44, s78, 5, v218
	v_lshlrev_b64 v[32:33], 14, v[202:203]
	v_lshl_add_u64 v[32:33], vcc, 0, v[32:33]
	v_lshlrev_b32_e32 v202, 2, v44
	v_lshl_add_u64 v[32:33], v[32:33], 0, v[202:203]
	s_movk_i32 s38, 0x4000
	v_add_co_u32_e32 v36, vcc, s38, v32
	s_nop 1
	v_addc_co_u32_e32 v37, vcc, 0, v33, vcc
	global_load_dwordx4 v[32:35], v[32:33], off nt
	s_nop 0
	global_load_dwordx4 v[36:39], v[36:37], off nt
	s_waitcnt vmcnt(10)
	s_waitcnt lgkmcnt(4)
	s_barrier
	s_setprio 1
	v_mfma_scale_f32_16x16x128_f8f6f4 v[188:191], v[24:31], v[46:53], v[188:191], v213, v213 op_sel_hi:[0,0,0]
	v_mfma_scale_f32_16x16x128_f8f6f4 v[184:187], v[16:23], v[46:53], v[184:187], v213, v213 op_sel_hi:[0,0,0]
	v_mfma_scale_f32_16x16x128_f8f6f4 v[180:183], v[24:31], v[54:61], v[180:183], v213, v213 op_sel_hi:[0,0,0]
	v_mfma_scale_f32_16x16x128_f8f6f4 v[176:179], v[16:23], v[54:61], v[176:179], v213, v213 op_sel_hi:[0,0,0]
	v_mfma_scale_f32_16x16x128_f8f6f4 v[172:175], v[24:31], v[192:199], v[172:175], v213, v213 op_sel_hi:[0,0,0]
	v_mfma_scale_f32_16x16x128_f8f6f4 v[168:171], v[16:23], v[192:199], v[168:171], v213, v213 op_sel_hi:[0,0,0]
	v_mfma_scale_f32_16x16x128_f8f6f4 v[164:167], v[24:31], v[220:227], v[164:167], v213, v213 op_sel_hi:[0,0,0]
	v_mfma_scale_f32_16x16x128_f8f6f4 v[160:163], v[16:23], v[220:227], v[160:163], v213, v213 op_sel_hi:[0,0,0]
	s_setprio 0
	s_setprio 1
	s_waitcnt lgkmcnt(2)
	v_mfma_scale_f32_16x16x128_f8f6f4 v[156:159], v[8:15], v[46:53], v[156:159], v213, v213 op_sel_hi:[0,0,0]
	s_waitcnt lgkmcnt(0)
	v_mfma_scale_f32_16x16x128_f8f6f4 v[152:155], v[0:7], v[46:53], v[152:155], v213, v213 op_sel_hi:[0,0,0]
	v_mfma_scale_f32_16x16x128_f8f6f4 v[148:151], v[8:15], v[54:61], v[148:151], v213, v213 op_sel_hi:[0,0,0]
	v_mfma_scale_f32_16x16x128_f8f6f4 v[144:147], v[0:7], v[54:61], v[144:147], v213, v213 op_sel_hi:[0,0,0]
	v_mfma_scale_f32_16x16x128_f8f6f4 v[140:143], v[8:15], v[192:199], v[140:143], v213, v213 op_sel_hi:[0,0,0]
	v_mfma_scale_f32_16x16x128_f8f6f4 v[136:139], v[0:7], v[192:199], v[136:139], v213, v213 op_sel_hi:[0,0,0]
	v_mfma_scale_f32_16x16x128_f8f6f4 v[132:135], v[8:15], v[220:227], v[132:135], v213, v213 op_sel_hi:[0,0,0]
	v_mfma_scale_f32_16x16x128_f8f6f4 v[128:131], v[0:7], v[220:227], v[128:131], v213, v213 op_sel_hi:[0,0,0]
	s_setprio 0
	s_barrier
	ds_read_b128 v[46:49], v216 offset:0x4000
	ds_read_b128 v[50:53], v216 offset:0x4400
	ds_read_b128 v[54:57], v216 offset:0x4800
	ds_read_b128 v[58:61], v216 offset:0x4c00
	ds_read_b128 v[192:195], v216 offset:0x5000
	ds_read_b128 v[196:199], v216 offset:0x5400
	ds_read_b128 v[220:223], v216 offset:0x5800
	ds_read_b128 v[224:227], v216 offset:0x5c00
	s_mov_b32 m0, s71
	s_nop 0
	buffer_load_dwordx4 v215, s[8:11], s16 offen lds
	s_add_i32 s38, s16, 0x80000
	s_mov_b32 m0, s72
	s_nop 0
	buffer_load_dwordx4 v215, s[8:11], s38 offen lds
	s_add_i32 s38, s16, 0x8000
	s_mov_b32 m0, s73
	s_nop 0
	buffer_load_dwordx4 v215, s[8:11], s38 offen lds
	s_add_i32 s38, s16, 0x88000
	s_mov_b32 m0, s74
	s_nop 0
	buffer_load_dwordx4 v215, s[8:11], s38 offen lds
	s_mov_b32 m0, s70
	s_add_i32 s38, s65, 0x40000
	buffer_load_dwordx4 v214, s[12:15], s65 offen lds
	s_mov_b32 m0, s75
	s_nop 0
	buffer_load_dwordx4 v214, s[12:15], s38 offen lds
	s_waitcnt vmcnt(10)
	s_waitcnt lgkmcnt(0)
	s_barrier
	s_setprio 1
	v_mfma_scale_f32_16x16x128_f8f6f4 v[124:127], v[24:31], v[46:53], v[124:127], v213, v213 op_sel_hi:[0,0,0]
	v_mfma_scale_f32_16x16x128_f8f6f4 v[120:123], v[16:23], v[46:53], v[120:123], v213, v213 op_sel_hi:[0,0,0]
	v_mfma_scale_f32_16x16x128_f8f6f4 v[116:119], v[24:31], v[54:61], v[116:119], v213, v213 op_sel_hi:[0,0,0]
	v_mfma_scale_f32_16x16x128_f8f6f4 v[112:115], v[16:23], v[54:61], v[112:115], v213, v213 op_sel_hi:[0,0,0]
	v_mfma_scale_f32_16x16x128_f8f6f4 v[108:111], v[24:31], v[192:199], v[108:111], v213, v213 op_sel_hi:[0,0,0]
	v_mfma_scale_f32_16x16x128_f8f6f4 v[104:107], v[16:23], v[192:199], v[104:107], v213, v213 op_sel_hi:[0,0,0]
	v_mfma_scale_f32_16x16x128_f8f6f4 v[100:103], v[24:31], v[220:227], v[100:103], v213, v213 op_sel_hi:[0,0,0]
	v_mfma_scale_f32_16x16x128_f8f6f4 v[96:99], v[16:23], v[220:227], v[96:99], v213, v213 op_sel_hi:[0,0,0]
	s_setprio 0
	s_setprio 1
	v_mfma_scale_f32_16x16x128_f8f6f4 v[92:95], v[8:15], v[46:53], v[92:95], v213, v213 op_sel_hi:[0,0,0]
	v_mfma_scale_f32_16x16x128_f8f6f4 v[88:91], v[0:7], v[46:53], v[88:91], v213, v213 op_sel_hi:[0,0,0]
	v_mfma_scale_f32_16x16x128_f8f6f4 v[84:87], v[8:15], v[54:61], v[84:87], v213, v213 op_sel_hi:[0,0,0]
	v_mfma_scale_f32_16x16x128_f8f6f4 v[80:83], v[0:7], v[54:61], v[80:83], v213, v213 op_sel_hi:[0,0,0]
	v_mfma_scale_f32_16x16x128_f8f6f4 v[76:79], v[8:15], v[192:199], v[76:79], v213, v213 op_sel_hi:[0,0,0]
	v_mfma_scale_f32_16x16x128_f8f6f4 v[72:75], v[0:7], v[192:199], v[72:75], v213, v213 op_sel_hi:[0,0,0]
	v_mfma_scale_f32_16x16x128_f8f6f4 v[68:71], v[8:15], v[220:227], v[68:71], v213, v213 op_sel_hi:[0,0,0]
	v_mfma_scale_f32_16x16x128_f8f6f4 v[64:67], v[0:7], v[220:227], v[64:67], v213, v213 op_sel_hi:[0,0,0]
	s_setprio 0
	s_barrier
	ds_read_b128 v[16:19], v217 offset:0x8000
	ds_read_b128 v[20:23], v217 offset:0x8400
	ds_read_b128 v[24:27], v217 offset:0x8800
	ds_read_b128 v[28:31], v217 offset:0x8c00
	ds_read_b128 v[46:49], v216 offset:0x8000
	ds_read_b128 v[50:53], v216 offset:0x8400
	ds_read_b128 v[54:57], v216 offset:0x8800
	ds_read_b128 v[58:61], v216 offset:0x8c00
	ds_read_b128 v[192:195], v216 offset:0x9000
	ds_read_b128 v[196:199], v216 offset:0x9400
	ds_read_b128 v[220:223], v216 offset:0x9800
	ds_read_b128 v[224:227], v216 offset:0x9c00
	ds_read_b128 v[8:11], v217 offset:0xc000
	ds_read_b128 v[12:15], v217 offset:0xc400
	ds_read_b128 v[0:3], v217 offset:0xc800
	ds_read_b128 v[4:7], v217 offset:0xcc00
	s_mov_b32 m0, s76
	s_add_i32 s38, s65, 0x80000
	buffer_load_dwordx4 v214, s[12:15], s38 offen lds
	s_add_i32 s38, s65, 0xc0000
	s_mov_b32 m0, s77
	s_nop 0
	buffer_load_dwordx4 v214, s[12:15], s38 offen lds
	s_waitcnt vmcnt(10)
	s_waitcnt lgkmcnt(4)
	s_barrier
	s_setprio 1
	v_mfma_scale_f32_16x16x128_f8f6f4 v[188:191], v[16:23], v[46:53], v[188:191], v213, v213 op_sel_hi:[0,0,0]
	v_mfma_scale_f32_16x16x128_f8f6f4 v[184:187], v[24:31], v[46:53], v[184:187], v213, v213 op_sel_hi:[0,0,0]
	v_mfma_scale_f32_16x16x128_f8f6f4 v[180:183], v[16:23], v[54:61], v[180:183], v213, v213 op_sel_hi:[0,0,0]
	v_mfma_scale_f32_16x16x128_f8f6f4 v[176:179], v[24:31], v[54:61], v[176:179], v213, v213 op_sel_hi:[0,0,0]
	v_mfma_scale_f32_16x16x128_f8f6f4 v[172:175], v[16:23], v[192:199], v[172:175], v213, v213 op_sel_hi:[0,0,0]
	v_mfma_scale_f32_16x16x128_f8f6f4 v[168:171], v[24:31], v[192:199], v[168:171], v213, v213 op_sel_hi:[0,0,0]
	v_mfma_scale_f32_16x16x128_f8f6f4 v[164:167], v[16:23], v[220:227], v[164:167], v213, v213 op_sel_hi:[0,0,0]
	v_mfma_scale_f32_16x16x128_f8f6f4 v[160:163], v[24:31], v[220:227], v[160:163], v213, v213 op_sel_hi:[0,0,0]
	s_setprio 0
	s_setprio 1
	s_waitcnt lgkmcnt(2)
	v_mfma_scale_f32_16x16x128_f8f6f4 v[156:159], v[8:15], v[46:53], v[156:159], v213, v213 op_sel_hi:[0,0,0]
	s_waitcnt lgkmcnt(0)
	v_mfma_scale_f32_16x16x128_f8f6f4 v[152:155], v[0:7], v[46:53], v[152:155], v213, v213 op_sel_hi:[0,0,0]
	v_mfma_scale_f32_16x16x128_f8f6f4 v[148:151], v[8:15], v[54:61], v[148:151], v213, v213 op_sel_hi:[0,0,0]
	v_mfma_scale_f32_16x16x128_f8f6f4 v[144:147], v[0:7], v[54:61], v[144:147], v213, v213 op_sel_hi:[0,0,0]
	v_mfma_scale_f32_16x16x128_f8f6f4 v[140:143], v[8:15], v[192:199], v[140:143], v213, v213 op_sel_hi:[0,0,0]
	v_mfma_scale_f32_16x16x128_f8f6f4 v[136:139], v[0:7], v[192:199], v[136:139], v213, v213 op_sel_hi:[0,0,0]
	v_mfma_scale_f32_16x16x128_f8f6f4 v[132:135], v[8:15], v[220:227], v[132:135], v213, v213 op_sel_hi:[0,0,0]
	v_mfma_scale_f32_16x16x128_f8f6f4 v[128:131], v[0:7], v[220:227], v[128:131], v213, v213 op_sel_hi:[0,0,0]
	s_setprio 0
	s_barrier
	ds_read_b128 v[46:49], v216 offset:0xc000
	ds_read_b128 v[50:53], v216 offset:0xc400
	ds_read_b128 v[54:57], v216 offset:0xc800
	ds_read_b128 v[58:61], v216 offset:0xcc00
	ds_read_b128 v[192:195], v216 offset:0xd000
	ds_read_b128 v[196:199], v216 offset:0xd400
	ds_read_b128 v[220:223], v216 offset:0xd800
	ds_read_b128 v[224:227], v216 offset:0xdc00
	s_mov_b32 m0, s80
	s_nop 0
	buffer_load_dwordx4 v215, s[8:11], s17 offen lds
	s_add_i32 s17, s16, 0x80080
	s_mov_b32 m0, s81
	s_add_i32 s65, s65, 0x40080
	buffer_load_dwordx4 v215, s[8:11], s17 offen lds
	s_add_i32 s17, s16, 0x8080
	s_mov_b32 m0, s84
	s_add_i32 s16, s16, 0x88080
	buffer_load_dwordx4 v215, s[8:11], s17 offen lds
	s_mov_b32 m0, s85
	s_nop 0
	buffer_load_dwordx4 v215, s[8:11], s16 offen lds
	s_mov_b32 m0, s82
	s_nop 0
	buffer_load_dwordx4 v214, s[12:15], s3 offen lds
	s_mov_b32 m0, s83
	s_nop 0
	buffer_load_dwordx4 v214, s[12:15], s65 offen lds
	s_waitcnt vmcnt(8)
	s_waitcnt lgkmcnt(0)
	s_barrier
	s_setprio 1
	v_mfma_scale_f32_16x16x128_f8f6f4 v[124:127], v[16:23], v[46:53], v[124:127], v213, v213 op_sel_hi:[0,0,0]
	v_mfma_scale_f32_16x16x128_f8f6f4 v[120:123], v[24:31], v[46:53], v[120:123], v213, v213 op_sel_hi:[0,0,0]
	v_mfma_scale_f32_16x16x128_f8f6f4 v[116:119], v[16:23], v[54:61], v[116:119], v213, v213 op_sel_hi:[0,0,0]
	v_mfma_scale_f32_16x16x128_f8f6f4 v[112:115], v[24:31], v[54:61], v[112:115], v213, v213 op_sel_hi:[0,0,0]
	v_mfma_scale_f32_16x16x128_f8f6f4 v[108:111], v[16:23], v[192:199], v[108:111], v213, v213 op_sel_hi:[0,0,0]
	v_mfma_scale_f32_16x16x128_f8f6f4 v[104:107], v[24:31], v[192:199], v[104:107], v213, v213 op_sel_hi:[0,0,0]
	v_mfma_scale_f32_16x16x128_f8f6f4 v[100:103], v[16:23], v[220:227], v[100:103], v213, v213 op_sel_hi:[0,0,0]
	v_mfma_scale_f32_16x16x128_f8f6f4 v[96:99], v[24:31], v[220:227], v[96:99], v213, v213 op_sel_hi:[0,0,0]
	s_setprio 0
	s_setprio 1
	v_mfma_scale_f32_16x16x128_f8f6f4 v[92:95], v[8:15], v[46:53], v[92:95], v213, v213 op_sel_hi:[0,0,0]
	v_mfma_scale_f32_16x16x128_f8f6f4 v[88:91], v[0:7], v[46:53], v[88:91], v213, v213 op_sel_hi:[0,0,0]
	v_mfma_scale_f32_16x16x128_f8f6f4 v[84:87], v[8:15], v[54:61], v[84:87], v213, v213 op_sel_hi:[0,0,0]
	v_mfma_scale_f32_16x16x128_f8f6f4 v[80:83], v[0:7], v[54:61], v[80:83], v213, v213 op_sel_hi:[0,0,0]
	v_mfma_scale_f32_16x16x128_f8f6f4 v[76:79], v[8:15], v[192:199], v[76:79], v213, v213 op_sel_hi:[0,0,0]
	v_mfma_scale_f32_16x16x128_f8f6f4 v[72:75], v[0:7], v[192:199], v[72:75], v213, v213 op_sel_hi:[0,0,0]
	v_mfma_scale_f32_16x16x128_f8f6f4 v[68:71], v[8:15], v[220:227], v[68:71], v213, v213 op_sel_hi:[0,0,0]
	v_mfma_scale_f32_16x16x128_f8f6f4 v[64:67], v[0:7], v[220:227], v[64:67], v213, v213 op_sel_hi:[0,0,0]
	s_setprio 0
	s_barrier
	s_bitcmp0_b32 s64, 0
	s_waitcnt vmcnt(15)
	v_mul_f32_e32 v0, 0x42800000, v32
	s_waitcnt vmcnt(14)
	v_mul_f32_e32 v4, 0x42800000, v36
	v_mul_f32_e32 v1, 0x42800000, v33
	v_mul_f32_e32 v5, 0x42800000, v37
	v_mul_f32_e32 v2, 0x42800000, v34
	v_mul_f32_e32 v6, 0x42800000, v38
	v_mul_f32_e32 v3, 0x42800000, v35
	v_mul_f32_e32 v7, 0x42800000, v39
	s_mov_b64 s[64:65], -1
	s_cbranch_scc0 .LBB0_929
	s_andn2_b64 vcc, exec, s[64:65]
	s_cbranch_vccnz .LBB0_925
	s_branch .LBB0_930
.LBB0_929:
	v_cvt_pk_fp8_f32 v40, v0, v4
	v_cvt_pk_fp8_f32 v41, v1, v5
	v_cvt_pk_fp8_f32 v42, v2, v6
	v_cvt_pk_fp8_f32 v43, v3, v7
	s_cbranch_execnz .LBB0_925

.LBB0_924:
.LBB0_925:
	s_addk_i32 s33, 0x100
	s_add_i32 s79, s79, 2
	s_cmpk_eq_i32 s33, 0xf00
	s_cbranch_scc0 .Lp6_top
	v_mov_b32_e32 v202, v40
	v_mov_b32_e32 v219, v41
	v_mov_b32_e32 v220, v42
	v_mov_b32_e32 v221, v43
